# PEER: one static s_setprio 1 for waves 4-7 (the second wave on each SIMD) for the whole token loop, reset at phase exit
# speedup vs baseline: 1.0058x; 1.0058x over previous
.LBB0_709:
	s_mul_i32 s8, s6, 0xab
	s_bfe_u32 s8, s8, 0x70009
	s_mul_i32 s8, s8, 3
	s_add_i32 s9, s6, -3
	s_sub_i32 s37, s6, s8
	s_cmp_lt_u32 s9, 3
	s_cselect_b32 s42, 0, 0x800
	s_cmp_gt_u32 s6, 2
	s_cselect_b64 s[8:9], -1, 0
	s_and_b64 s[40:41], s[8:9], exec
	s_cselect_b32 s40, s42, 0x2800
	s_and_b64 s[8:9], s[96:97], s[8:9]
	v_cndmask_b32_e64 v8, 0, 1, s[8:9]
	s_and_b32 s8, s37, 0xff
	v_readfirstlane_b32 s9, v8
	s_add_i32 s9, s36, s9
	s_mul_i32 s9, s9, 3
	s_add_i32 s8, s9, s8
	s_mul_hi_u32 s9, s8, 0xc000
	s_mul_i32 s8, s8, 0xc000
	s_add_u32 s8, s4, s8
	s_addc_u32 s9, s5, s9
	s_lshl_b32 s37, s40, 2
	s_add_u32 s8, s8, s37
	s_addc_u32 s9, s9, 0
	v_lshl_add_u64 v[8:9], v[4:5], 2, s[8:9]
	global_load_dwordx4 v[8:11], v[8:9], off
	s_add_i32 s6, s6, 1
	s_cmp_eq_u32 s6, 9
	s_waitcnt vmcnt(0)
	ds_write_b128 v7, v[8:11]
	v_add_u32_e32 v7, 0x2000, v7
	s_cbranch_scc0 .LBB0_709
	s_load_dwordx4 s[40:43], s[0:1], 0x90
	s_lshl_b32 s6, s36, 11
	s_lshl_b64 s[4:5], s[6:7], 2
	v_lshlrev_b64 v[8:9], 2, v[4:5]
	v_add_u32_e32 v10, 0, v6
	s_waitcnt lgkmcnt(0)
	s_add_u32 s8, s40, s4
	s_addc_u32 s9, s41, s5
	v_lshl_add_u64 v[4:5], s[8:9], 0, v[8:9]
	global_load_dwordx4 v[4:7], v[4:5], off
	s_add_u32 s4, s42, s4
	v_add_u32_e32 v11, 0x1c200, v10
	s_addc_u32 s5, s43, s5
	s_lshl_b32 s6, s36, 6
	v_and_b32_e32 v21, 63, v2
	v_cmp_eq_u32_e64 s[40:41], 0, v21
	s_waitcnt vmcnt(0)
	ds_write_b128 v11, v[4:7]
	v_lshl_add_u64 v[4:5], s[4:5], 0, v[8:9]
	global_load_dwordx4 v[4:7], v[4:5], off
	s_lshl_b64 s[4:5], s[6:7], 2
	v_readlane_b32 s6, v254, 50
	v_add_u32_e32 v8, 0x1e200, v10
	s_add_u32 s66, s6, s4
	v_readlane_b32 s4, v254, 51
	s_addc_u32 s67, s4, s5
	s_waitcnt vmcnt(0)
	ds_write_b128 v8, v[4:7]
	v_mov_b32_e32 v4, 0
	s_waitcnt lgkmcnt(0)
	s_barrier
	v_readlane_b32 s6, v254, 3
	s_lshr_b32 s4, s27, 6
	s_cmp_gt_u32 s4, 3
	s_cbranch_scc0 .Lpe_lowprio
	s_setprio 1
.Lpe_lowprio:
	s_nop 0
	s_add_i32 s6, s6, s4
	v_readlane_b32 s44, v253, 31
	v_readlane_b32 s45, v253, 32
	s_mov_b32 s88, s6
	s_cmp_lt_i32 s88, s26
	v_lshlrev_b32_e32 v20, 6, v21
	s_cselect_b64 s[4:5], -1, 0
	s_cmp_ge_i32 s88, s26
	v_and_b32_e32 v24, 0xf00, v20
	v_and_b32_e32 v22, 0xc0, v20
	s_cbranch_scc1 .LBB0_716
	s_ashr_i32 s89, s88, 31
	s_lshl_b64 s[8:9], s[88:89], 12
	s_add_u32 s8, s50, s8
	s_addc_u32 s9, s51, s9
	v_mov_b32_e32 v25, v3
	v_lshl_add_u64 v[4:5], s[8:9], 0, v[24:25]
	v_mov_b32_e32 v23, v3
	v_lshl_add_u64 v[4:5], v[4:5], 0, v[22:23]
	s_mov_b64 s[8:9], 0x24d00000
	s_mov_b32 s6, 0x24d00000
	v_lshl_add_u64 v[16:17], v[4:5], 0, s[8:9]
	v_add_co_u32_e32 v4, vcc, s6, v4
	s_nop 1
	v_addc_co_u32_e32 v5, vcc, 0, v5, vcc
	global_load_dwordx4 v[4:7], v[4:5], off
	s_nop 0
	global_load_dwordx4 v[8:11], v[16:17], off offset:48
	global_load_dwordx4 v[12:15], v[16:17], off offset:32
	s_nop 0
	global_load_dwordx4 v[16:19], v[16:17], off offset:16

.LBB0_798:
	s_setprio 0
	v_readlane_b32 s0, v253, 33
	v_readlane_b32 s84, v253, 20
	s_add_i32 s0, s0, 8
	v_readlane_b32 s96, v253, 18
	v_readlane_b32 s85, v253, 21
	v_readlane_b32 s86, v253, 23
	v_readlane_b32 s88, v253, 25
	v_readlane_b32 s64, v253, 27
	v_readlane_b32 s66, v253, 29
	s_cmp_ge_i32 s0, s69
	v_readlane_b32 s97, v253, 19
	v_readlane_b32 s76, v253, 22
	v_readlane_b32 s87, v253, 24
	v_readlane_b32 s89, v253, 26
	v_readlane_b32 s65, v253, 28
	v_readlane_b32 s67, v253, 30
	v_readlane_b32 s85, v253, 34
	s_cbranch_scc1 .LBB0_232
	s_waitcnt vmcnt(0)
	s_barrier
	s_mov_b64 s[0:1], exec
	v_readlane_b32 s4, v253, 16
	v_readlane_b32 s5, v253, 17
	s_and_b64 s[4:5], s[0:1], s[4:5]
	s_mov_b64 exec, s[4:5]
	s_cbranch_execz .LBB0_231
	v_readlane_b32 s4, v254, 2
	s_waitcnt vmcnt(0) expcnt(0) lgkmcnt(0)
	s_nop 0
	v_mov_b32_e32 v2, s4
	ds_read_b32 v5, v2
	ds_read_b32 v4, v2 offset:4
	s_waitcnt lgkmcnt(1)
	v_cmp_ne_u32_e32 vcc, 0, v5
	s_cbranch_vccnz .LBB0_815
	v_readlane_b32 s8, v254, 0
	v_readlane_b32 s9, v254, 1
	s_load_dwordx2 s[4:5], s[8:9], 0x4
	s_mov_b32 s26, 1
	s_waitcnt lgkmcnt(0)
	s_mul_i32 s6, s4, s33
	s_mul_i32 s6, s6, s5
	s_branch .LBB0_803
